# P0 rmsnorm x loads nt (on top of P1 + conversion nt stores)
# speedup vs baseline: 1.0166x; 1.0166x over previous
.LBB0_85:
	s_ashr_i32 s1, s0, 31
	s_lshl_b64 s[2:3], s[0:1], 12
	v_lshl_add_u64 v[18:19], v[42:43], 0, s[2:3]
	s_add_i32 s6, s0, s5
	global_load_dwordx4 v[56:59], v[18:19], off nt
	global_load_dwordx4 v[34:37], v[18:19], off offset:1024 nt
	global_load_dwordx4 v[26:29], v[18:19], off offset:2048 nt
	s_ashr_i32 s7, s6, 31
	global_load_dwordx4 v[18:21], v[18:19], off offset:3072 nt
	s_lshl_b64 s[2:3], s[6:7], 12
	v_lshl_add_u64 v[22:23], v[42:43], 0, s[2:3]
	global_load_dwordx4 v[60:63], v[22:23], off nt
	global_load_dwordx4 v[38:41], v[22:23], off offset:1024 nt
	global_load_dwordx4 v[30:33], v[22:23], off offset:2048 nt
	s_nop 0
	global_load_dwordx4 v[22:25], v[22:23], off offset:3072 nt
	s_lshl_b64 s[8:9], s[0:1], 10
	s_lshl_b64 s[10:11], s[6:7], 10
	s_waitcnt vmcnt(7)
	v_mul_f32_e32 v55, v57, v57
	v_mul_f32_e32 v64, v59, v59
	s_waitcnt vmcnt(6)
	v_mul_f32_e32 v65, v35, v35
	v_mul_f32_e32 v67, v37, v37
	s_waitcnt vmcnt(5)
	v_mul_f32_e32 v70, v27, v27
	v_mul_f32_e32 v71, v29, v29
	v_fmac_f32_e32 v55, v56, v56
	v_fmac_f32_e32 v64, v58, v58
	v_fmac_f32_e32 v65, v34, v34
	v_fmac_f32_e32 v67, v36, v36
	s_waitcnt vmcnt(4)
	v_mul_f32_e32 v72, v19, v19
	v_mul_f32_e32 v73, v21, v21
	s_waitcnt vmcnt(3)
	v_mul_f32_e32 v74, v61, v61
	v_mul_f32_e32 v75, v63, v63
	s_waitcnt vmcnt(2)
	v_mul_f32_e32 v76, v39, v39
	v_mul_f32_e32 v77, v41, v41
	v_fmac_f32_e32 v70, v26, v26
	v_fmac_f32_e32 v71, v28, v28
	v_add_f32_e32 v55, v55, v64
	v_add_f32_e32 v64, v65, v67
	s_waitcnt vmcnt(1)
	v_mul_f32_e32 v78, v31, v31
	v_mul_f32_e32 v79, v33, v33
	v_fmac_f32_e32 v72, v18, v18
	v_fmac_f32_e32 v73, v20, v20
	v_fmac_f32_e32 v74, v60, v60
	v_fmac_f32_e32 v75, v62, v62
	v_fmac_f32_e32 v76, v38, v38
	v_fmac_f32_e32 v77, v40, v40
	v_add_f32_e32 v65, v70, v71
	v_add_f32_e32 v55, v55, v64
	s_waitcnt vmcnt(0)
	v_mul_f32_e32 v80, v23, v23
	v_mul_f32_e32 v81, v25, v25
	v_fmac_f32_e32 v78, v30, v30
	v_fmac_f32_e32 v79, v32, v32
	v_add_f32_e32 v67, v72, v73
	v_add_f32_e32 v70, v74, v75
	v_add_f32_e32 v64, v76, v77
	v_add_f32_e32 v55, v55, v65
	v_fmac_f32_e32 v80, v22, v22
	v_fmac_f32_e32 v81, v24, v24
	v_add_f32_e32 v71, v78, v79
	v_add_f32_e32 v64, v70, v64
	v_add_f32_e32 v55, v55, v67
	v_add_f32_e32 v72, v80, v81
	v_add_f32_e32 v64, v64, v71
	ds_bpermute_b32 v65, v46, v55
	v_add_f32_e32 v64, v64, v72
	ds_bpermute_b32 v67, v46, v64
	s_waitcnt lgkmcnt(1)
	v_add_f32_e32 v55, v55, v65
	ds_bpermute_b32 v65, v47, v55
	s_waitcnt lgkmcnt(1)
	v_add_f32_e32 v64, v64, v67
	ds_bpermute_b32 v67, v47, v64
	s_waitcnt lgkmcnt(1)
	v_add_f32_e32 v55, v55, v65
	ds_bpermute_b32 v65, v48, v55
	s_waitcnt lgkmcnt(1)
	v_add_f32_e32 v64, v64, v67
	ds_bpermute_b32 v67, v48, v64
	s_waitcnt lgkmcnt(1)
	v_add_f32_e32 v55, v55, v65
	ds_bpermute_b32 v65, v49, v55
	s_waitcnt lgkmcnt(1)
	v_add_f32_e32 v64, v64, v67
	ds_bpermute_b32 v67, v49, v64
	s_waitcnt lgkmcnt(1)
	v_add_f32_e32 v55, v55, v65
	ds_bpermute_b32 v65, v50, v55
	s_waitcnt lgkmcnt(1)
	v_add_f32_e32 v64, v64, v67
	ds_bpermute_b32 v67, v50, v64
	s_waitcnt lgkmcnt(1)
	v_add_f32_e32 v55, v55, v65
	ds_bpermute_b32 v65, v51, v55
	s_waitcnt lgkmcnt(1)
	v_add_f32_e32 v64, v64, v67
	ds_bpermute_b32 v67, v51, v64
	s_waitcnt lgkmcnt(1)
	v_add_f32_e32 v55, v55, v65
	v_fmamk_f32 v55, v55, 0x3a800000, v52
	s_waitcnt lgkmcnt(0)
	v_add_f32_e32 v64, v64, v67
	v_mul_f32_e32 v65, 0x4f800000, v55
	v_cmp_gt_f32_e32 vcc, s12, v55
	v_fmamk_f32 v64, v64, 0x3a800000, v52
	v_cmp_gt_f32_e64 s[0:1], s12, v64
	v_cndmask_b32_e32 v55, v55, v65, vcc
	v_mul_f32_e32 v65, 0x4f800000, v64
	v_sqrt_f32_e32 v67, v55
	v_cndmask_b32_e64 v64, v64, v65, s[0:1]
	v_sqrt_f32_e32 v65, v64
	v_add_u32_e32 v70, -1, v67
	v_add_u32_e32 v71, 1, v67
	v_fma_f32 v72, -v70, v67, v55
	v_fma_f32 v73, -v71, v67, v55
	v_add_u32_e32 v74, -1, v65
	v_cmp_ge_f32_e64 s[2:3], 0, v72
	v_add_u32_e32 v75, 1, v65
	v_fma_f32 v72, -v75, v65, v64
	v_cndmask_b32_e64 v67, v67, v70, s[2:3]
	v_fma_f32 v70, -v74, v65, v64
	v_cmp_lt_f32_e64 s[2:3], 0, v73
	s_nop 1
	v_cndmask_b32_e64 v67, v67, v71, s[2:3]
	v_cmp_ge_f32_e64 s[2:3], 0, v70
	v_mul_f32_e32 v70, 0x37800000, v67
	v_cndmask_b32_e32 v67, v67, v70, vcc
	v_cndmask_b32_e64 v65, v65, v74, s[2:3]
	v_cmp_lt_f32_e64 s[2:3], 0, v72
	v_cmp_class_f32_e32 vcc, v55, v53
	s_nop 0
	v_cndmask_b32_e64 v65, v65, v75, s[2:3]
	v_mul_f32_e32 v70, 0x37800000, v65
	v_cndmask_b32_e32 v55, v67, v55, vcc
	v_cndmask_b32_e64 v65, v65, v70, s[0:1]
	v_div_scale_f32 v67, s[0:1], v55, v55, 1.0
	v_cmp_class_f32_e64 s[0:1], v64, v53
	v_div_scale_f32 v70, vcc, 1.0, v55, 1.0
	s_nop 0
	v_cndmask_b32_e64 v64, v65, v64, s[0:1]
	v_rcp_f32_e32 v65, v67
	v_div_scale_f32 v71, s[0:1], v64, v64, 1.0
	v_rcp_f32_e32 v72, v71
	v_fma_f32 v74, -v67, v65, 1.0
	v_fmac_f32_e32 v65, v74, v65
	v_div_scale_f32 v73, s[0:1], 1.0, v64, 1.0
	v_fma_f32 v74, -v71, v72, 1.0
	v_mul_f32_e32 v75, v70, v65
	v_fmac_f32_e32 v72, v74, v72
	v_fma_f32 v74, -v67, v75, v70
	v_mul_f32_e32 v76, v73, v72
	v_fmac_f32_e32 v75, v74, v65
	v_fma_f32 v74, -v71, v76, v73
	v_fma_f32 v67, -v67, v75, v70
	v_fmac_f32_e32 v76, v74, v72
	v_div_fmas_f32 v65, v67, v65, v75
	v_fma_f32 v67, -v71, v76, v73
	s_mov_b64 vcc, s[0:1]
	v_div_fixup_f32 v55, v65, v55, 1.0
	v_div_fmas_f32 v65, v67, v72, v76
	v_div_fixup_f32 v65, v65, v64, 1.0
	v_mul_f32_e32 v64, 0x41800000, v55
	v_pk_mul_f32 v[56:57], v[56:57], v[64:65] op_sel_hi:[1,0]
	v_mul_f32_e32 v70, 0x41800000, v65
	v_pk_mul_f32 v[56:57], v[2:3], v[56:57]
	v_pk_mul_f32 v[58:59], v[58:59], v[64:65] op_sel_hi:[1,0]
	v_med3_f32 v55, v56, s13, v54
	v_med3_f32 v56, v57, s13, v54
	v_mov_b32_e32 v65, 0
	v_cvt_pk_fp8_f32 v65, v55, v56
	v_pk_mul_f32 v[58:59], v[4:5], v[58:59]
	v_pk_mul_f32 v[60:61], v[60:61], v[70:71] op_sel_hi:[1,0]
	v_med3_f32 v55, v58, s13, v54
	v_med3_f32 v56, v59, s13, v54
	v_pk_mul_f32 v[60:61], v[2:3], v[60:61]
	v_cvt_pk_fp8_f32 v65, v55, v56 op_sel:[0,0,1]
	v_med3_f32 v57, v60, s13, v54
	v_med3_f32 v58, v61, s13, v54
	v_mov_b32_e32 v60, 0
	v_cvt_pk_fp8_f32 v60, v57, v58
	v_pk_mul_f32 v[62:63], v[62:63], v[70:71] op_sel_hi:[1,0]
	v_pk_mul_f32 v[34:35], v[34:35], v[64:65] op_sel_hi:[1,0]
	v_pk_mul_f32 v[62:63], v[4:5], v[62:63]
	v_pk_mul_f32 v[36:37], v[36:37], v[64:65] op_sel_hi:[1,0]
	v_med3_f32 v55, v62, s13, v54
	v_med3_f32 v56, v63, s13, v54
	v_pk_mul_f32 v[34:35], v[6:7], v[34:35]
	v_pk_mul_f32 v[38:39], v[38:39], v[70:71] op_sel_hi:[1,0]
	v_cvt_pk_fp8_f32 v60, v55, v56 op_sel:[0,0,1]
	v_pk_mul_f32 v[36:37], v[8:9], v[36:37]
	v_pk_mul_f32 v[38:39], v[6:7], v[38:39]
	v_med3_f32 v34, v34, s13, v54
	v_med3_f32 v35, v35, s13, v54
	v_mov_b32_e32 v55, 0
	v_cvt_pk_fp8_f32 v55, v34, v35
	v_med3_f32 v34, v36, s13, v54
	v_med3_f32 v35, v37, s13, v54
	v_med3_f32 v36, v38, s13, v54
	v_med3_f32 v37, v39, s13, v54
	v_mov_b32_e32 v38, 0
	v_cvt_pk_fp8_f32 v38, v36, v37
	v_pk_mul_f32 v[40:41], v[40:41], v[70:71] op_sel_hi:[1,0]
	v_pk_mul_f32 v[26:27], v[26:27], v[64:65] op_sel_hi:[1,0]
	v_pk_mul_f32 v[40:41], v[8:9], v[40:41]
	v_cvt_pk_fp8_f32 v55, v34, v35 op_sel:[0,0,1]
	v_med3_f32 v34, v40, s13, v54
	v_med3_f32 v35, v41, s13, v54
	v_pk_mul_f32 v[28:29], v[28:29], v[64:65] op_sel_hi:[1,0]
	v_pk_mul_f32 v[26:27], v[10:11], v[26:27]
	v_pk_mul_f32 v[30:31], v[30:31], v[70:71] op_sel_hi:[1,0]
	v_cvt_pk_fp8_f32 v38, v34, v35 op_sel:[0,0,1]
	v_pk_mul_f32 v[28:29], v[12:13], v[28:29]
	v_pk_mul_f32 v[30:31], v[10:11], v[30:31]
	v_med3_f32 v26, v26, s13, v54
	v_med3_f32 v27, v27, s13, v54
	v_mov_b32_e32 v34, 0
	v_cvt_pk_fp8_f32 v34, v26, v27
	v_med3_f32 v26, v28, s13, v54
	v_med3_f32 v27, v29, s13, v54
	v_med3_f32 v28, v30, s13, v54
	v_med3_f32 v29, v31, s13, v54
	v_mov_b32_e32 v30, 0
	v_cvt_pk_fp8_f32 v30, v28, v29
	v_pk_mul_f32 v[32:33], v[32:33], v[70:71] op_sel_hi:[1,0]
	v_pk_mul_f32 v[18:19], v[18:19], v[64:65] op_sel_hi:[1,0]
	v_pk_mul_f32 v[32:33], v[12:13], v[32:33]
	v_cvt_pk_fp8_f32 v34, v26, v27 op_sel:[0,0,1]
	v_med3_f32 v26, v32, s13, v54
	v_med3_f32 v27, v33, s13, v54
	v_pk_mul_f32 v[20:21], v[20:21], v[64:65] op_sel_hi:[1,0]
	v_pk_mul_f32 v[18:19], v[14:15], v[18:19]
	v_pk_mul_f32 v[22:23], v[22:23], v[70:71] op_sel_hi:[1,0]
	v_cvt_pk_fp8_f32 v30, v26, v27 op_sel:[0,0,1]
	v_pk_mul_f32 v[20:21], v[16:17], v[20:21]
	v_pk_mul_f32 v[22:23], v[14:15], v[22:23]
	v_med3_f32 v18, v18, s13, v54
	v_med3_f32 v19, v19, s13, v54
	v_mov_b32_e32 v26, 0
	v_cvt_pk_fp8_f32 v26, v18, v19
	v_med3_f32 v18, v20, s13, v54
	v_med3_f32 v19, v21, s13, v54
	v_med3_f32 v20, v22, s13, v54
	v_med3_f32 v21, v23, s13, v54
	v_mov_b32_e32 v22, 0
	v_cvt_pk_fp8_f32 v22, v20, v21
	v_pk_mul_f32 v[24:25], v[24:25], v[70:71] op_sel_hi:[1,0]
	v_cvt_pk_fp8_f32 v26, v18, v19 op_sel:[0,0,1]
	v_pk_mul_f32 v[24:25], v[16:17], v[24:25]
	s_add_i32 s0, s6, s5
	v_med3_f32 v18, v24, s13, v54
	v_med3_f32 v19, v25, s13, v54
	v_cvt_pk_fp8_f32 v22, v18, v19 op_sel:[0,0,1]
	v_lshl_add_u64 v[56:57], v[44:45], 0, s[8:9]
	v_lshl_add_u64 v[58:59], v[44:45], 0, s[10:11]
	s_cmpk_gt_i32 s0, 0x7fff
	global_store_dword v[56:57], v65, off
	global_store_dword v[58:59], v60, off
	global_store_dword v[56:57], v55, off offset:256
	global_store_dword v[58:59], v38, off offset:256
	global_store_dword v[56:57], v34, off offset:512
	global_store_dword v[58:59], v30, off offset:512
	global_store_dword v[56:57], v26, off offset:768
	global_store_dword v[58:59], v22, off offset:768
	s_cbranch_scc0 .LBB0_85
